# v10 with all P2 GEMM output stores as sc1 (write-through)
# baseline (speedup 1.0000x reference)
.LBB0_293:
	s_lshl_b32 s18, s54, 8
	s_add_i32 s19, s18, 0x800
	s_cmp_lt_i32 s54, 24
	s_cselect_b32 s18, s18, s19
	v_or_b32_e32 v4, s18, v200
	v_ashrrev_i32_e32 v5, 31, v4
	v_mov_b64_e32 v[2:3], s[0:1]
	v_mad_i64_i32 v[8:9], s[58:59], v6, s35, v[2:3]
	v_lshlrev_b64 v[4:5], 1, v[4:5]
	v_lshl_add_u64 v[12:13], v[8:9], 0, v[4:5]
	v_pk_mul_f32 v[8:9], v[158:159], s[38:39] op_sel_hi:[1,0]
	v_pk_mul_f32 v[10:11], v[160:161], s[38:39] op_sel_hi:[1,0]
	v_cvt_pk_bf16_f32 v8, v8, v9
	v_pk_mul_f32 v[14:15], v[156:157], s[38:39] op_sel_hi:[1,0]
	v_cvt_pk_bf16_f32 v9, v10, v11
	v_pk_mul_f32 v[16:17], v[154:155], s[38:39] op_sel_hi:[1,0]
	v_or_b32_e32 v7, 16, v6
	v_cvt_pk_bf16_f32 v10, v16, v17
	v_cvt_pk_bf16_f32 v11, v14, v15
	global_store_dwordx4 v[12:13], v[8:11], off sc1
	v_pk_mul_f32 v[14:15], v[140:141], s[38:39] op_sel_hi:[1,0]
	v_pk_mul_f32 v[16:17], v[138:139], s[38:39] op_sel_hi:[1,0]
	v_pk_mul_f32 v[8:9], v[142:143], s[38:39] op_sel_hi:[1,0]
	v_pk_mul_f32 v[10:11], v[144:145], s[38:39] op_sel_hi:[1,0]
	v_cvt_pk_bf16_f32 v8, v8, v9
	s_nop 0
	v_cvt_pk_bf16_f32 v9, v10, v11
	v_cvt_pk_bf16_f32 v10, v16, v17
	v_cvt_pk_bf16_f32 v11, v14, v15
	global_store_dwordx4 v[12:13], v[8:11], off offset:256 sc1
	v_pk_mul_f32 v[14:15], v[148:149], s[38:39] op_sel_hi:[1,0]
	v_pk_mul_f32 v[16:17], v[146:147], s[38:39] op_sel_hi:[1,0]
	v_mad_i64_i32 v[8:9], s[58:59], v7, s35, v[2:3]
	v_lshl_add_u64 v[12:13], v[8:9], 0, v[4:5]
	v_pk_mul_f32 v[8:9], v[150:151], s[38:39] op_sel_hi:[1,0]
	v_pk_mul_f32 v[10:11], v[152:153], s[38:39] op_sel_hi:[1,0]
	v_cvt_pk_bf16_f32 v8, v8, v9
	v_or_b32_e32 v7, 32, v6
	v_cvt_pk_bf16_f32 v9, v10, v11
	v_cvt_pk_bf16_f32 v10, v16, v17
	v_cvt_pk_bf16_f32 v11, v14, v15
	global_store_dwordx4 v[12:13], v[8:11], off sc1
	v_pk_mul_f32 v[14:15], v[128:129], s[38:39] op_sel_hi:[1,0]
	v_pk_mul_f32 v[16:17], v[126:127], s[38:39] op_sel_hi:[1,0]
	v_pk_mul_f32 v[8:9], v[134:135], s[38:39] op_sel_hi:[1,0]
	v_pk_mul_f32 v[10:11], v[136:137], s[38:39] op_sel_hi:[1,0]
	v_cvt_pk_bf16_f32 v8, v8, v9
	s_nop 0
	v_cvt_pk_bf16_f32 v9, v10, v11
	v_cvt_pk_bf16_f32 v10, v16, v17
	v_cvt_pk_bf16_f32 v11, v14, v15
	global_store_dwordx4 v[12:13], v[8:11], off offset:256 sc1
	v_pk_mul_f32 v[14:15], v[124:125], s[38:39] op_sel_hi:[1,0]
	v_pk_mul_f32 v[16:17], v[122:123], s[38:39] op_sel_hi:[1,0]
	v_mad_i64_i32 v[8:9], s[58:59], v7, s35, v[2:3]
	v_lshl_add_u64 v[12:13], v[8:9], 0, v[4:5]
	v_pk_mul_f32 v[8:9], v[130:131], s[38:39] op_sel_hi:[1,0]
	v_pk_mul_f32 v[10:11], v[132:133], s[38:39] op_sel_hi:[1,0]
	v_cvt_pk_bf16_f32 v8, v8, v9
	v_or_b32_e32 v7, 48, v6
	v_cvt_pk_bf16_f32 v9, v10, v11
	v_cvt_pk_bf16_f32 v10, v16, v17
	v_cvt_pk_bf16_f32 v11, v14, v15
	global_store_dwordx4 v[12:13], v[8:11], off sc1
	v_pk_mul_f32 v[14:15], v[108:109], s[38:39] op_sel_hi:[1,0]
	v_pk_mul_f32 v[16:17], v[106:107], s[38:39] op_sel_hi:[1,0]
	v_pk_mul_f32 v[8:9], v[110:111], s[38:39] op_sel_hi:[1,0]
	v_pk_mul_f32 v[10:11], v[112:113], s[38:39] op_sel_hi:[1,0]
	v_cvt_pk_bf16_f32 v8, v8, v9
	s_nop 0
	v_cvt_pk_bf16_f32 v9, v10, v11
	v_cvt_pk_bf16_f32 v10, v16, v17
	v_cvt_pk_bf16_f32 v11, v14, v15
	global_store_dwordx4 v[12:13], v[8:11], off offset:256 sc1
	v_pk_mul_f32 v[14:15], v[116:117], s[38:39] op_sel_hi:[1,0]
	v_pk_mul_f32 v[16:17], v[114:115], s[38:39] op_sel_hi:[1,0]
	v_mad_i64_i32 v[8:9], s[58:59], v7, s35, v[2:3]
	v_lshl_add_u64 v[12:13], v[8:9], 0, v[4:5]
	v_pk_mul_f32 v[8:9], v[118:119], s[38:39] op_sel_hi:[1,0]
	v_pk_mul_f32 v[10:11], v[120:121], s[38:39] op_sel_hi:[1,0]
	v_cvt_pk_bf16_f32 v8, v8, v9
	v_add_u32_e32 v7, 0x80, v6
	v_cvt_pk_bf16_f32 v9, v10, v11
	v_cvt_pk_bf16_f32 v10, v16, v17
	v_cvt_pk_bf16_f32 v11, v14, v15
	global_store_dwordx4 v[12:13], v[8:11], off sc1
	v_pk_mul_f32 v[14:15], v[100:101], s[38:39] op_sel_hi:[1,0]
	v_pk_mul_f32 v[16:17], v[98:99], s[38:39] op_sel_hi:[1,0]
	v_pk_mul_f32 v[8:9], v[102:103], s[38:39] op_sel_hi:[1,0]
	v_pk_mul_f32 v[10:11], v[104:105], s[38:39] op_sel_hi:[1,0]
	v_cvt_pk_bf16_f32 v8, v8, v9
	s_nop 0
	v_cvt_pk_bf16_f32 v9, v10, v11
	v_cvt_pk_bf16_f32 v10, v16, v17
	v_cvt_pk_bf16_f32 v11, v14, v15
	global_store_dwordx4 v[12:13], v[8:11], off offset:256 sc1
	v_pk_mul_f32 v[14:15], v[92:93], s[38:39] op_sel_hi:[1,0]
	v_pk_mul_f32 v[16:17], v[90:91], s[38:39] op_sel_hi:[1,0]
	v_mad_i64_i32 v[8:9], s[58:59], v7, s35, v[2:3]
	v_lshl_add_u64 v[12:13], v[8:9], 0, v[4:5]
	v_pk_mul_f32 v[8:9], v[94:95], s[38:39] op_sel_hi:[1,0]
	v_pk_mul_f32 v[10:11], v[96:97], s[38:39] op_sel_hi:[1,0]
	v_cvt_pk_bf16_f32 v8, v8, v9
	v_add_u32_e32 v7, 0x90, v6
	v_cvt_pk_bf16_f32 v9, v10, v11
	v_cvt_pk_bf16_f32 v10, v16, v17
	v_cvt_pk_bf16_f32 v11, v14, v15
	global_store_dwordx4 v[12:13], v[8:11], off sc1
	v_pk_mul_f32 v[14:15], v[76:77], s[38:39] op_sel_hi:[1,0]
	v_pk_mul_f32 v[16:17], v[74:75], s[38:39] op_sel_hi:[1,0]
	v_pk_mul_f32 v[8:9], v[78:79], s[38:39] op_sel_hi:[1,0]
	v_pk_mul_f32 v[10:11], v[80:81], s[38:39] op_sel_hi:[1,0]
	v_cvt_pk_bf16_f32 v8, v8, v9
	s_nop 0
	v_cvt_pk_bf16_f32 v9, v10, v11
	v_cvt_pk_bf16_f32 v10, v16, v17
	v_cvt_pk_bf16_f32 v11, v14, v15
	global_store_dwordx4 v[12:13], v[8:11], off offset:256 sc1
	v_pk_mul_f32 v[14:15], v[84:85], s[38:39] op_sel_hi:[1,0]
	v_pk_mul_f32 v[16:17], v[82:83], s[38:39] op_sel_hi:[1,0]
	v_mad_i64_i32 v[8:9], s[58:59], v7, s35, v[2:3]
	v_lshl_add_u64 v[12:13], v[8:9], 0, v[4:5]
	v_pk_mul_f32 v[8:9], v[86:87], s[38:39] op_sel_hi:[1,0]
	v_pk_mul_f32 v[10:11], v[88:89], s[38:39] op_sel_hi:[1,0]
	v_cvt_pk_bf16_f32 v8, v8, v9
	v_add_u32_e32 v7, 0xa0, v6
	v_cvt_pk_bf16_f32 v9, v10, v11
	v_cvt_pk_bf16_f32 v10, v16, v17
	v_cvt_pk_bf16_f32 v11, v14, v15
	global_store_dwordx4 v[12:13], v[8:11], off sc1
	v_pk_mul_f32 v[14:15], v[64:65], s[38:39] op_sel_hi:[1,0]
	v_pk_mul_f32 v[16:17], v[62:63], s[38:39] op_sel_hi:[1,0]
	v_pk_mul_f32 v[8:9], v[70:71], s[38:39] op_sel_hi:[1,0]
	v_pk_mul_f32 v[10:11], v[72:73], s[38:39] op_sel_hi:[1,0]
	v_cvt_pk_bf16_f32 v8, v8, v9
	s_nop 0
	v_cvt_pk_bf16_f32 v9, v10, v11
	v_cvt_pk_bf16_f32 v10, v16, v17
	v_cvt_pk_bf16_f32 v11, v14, v15
	global_store_dwordx4 v[12:13], v[8:11], off offset:256 sc1
	v_pk_mul_f32 v[14:15], v[60:61], s[38:39] op_sel_hi:[1,0]
	v_pk_mul_f32 v[16:17], v[58:59], s[38:39] op_sel_hi:[1,0]
	v_mad_i64_i32 v[8:9], s[58:59], v7, s35, v[2:3]
	v_lshl_add_u64 v[12:13], v[8:9], 0, v[4:5]
	v_pk_mul_f32 v[8:9], v[66:67], s[38:39] op_sel_hi:[1,0]
	v_pk_mul_f32 v[10:11], v[68:69], s[38:39] op_sel_hi:[1,0]
	v_cvt_pk_bf16_f32 v8, v8, v9
	v_add_u32_e32 v7, 0xb0, v6
	v_cvt_pk_bf16_f32 v9, v10, v11
	v_cvt_pk_bf16_f32 v10, v16, v17
	v_cvt_pk_bf16_f32 v11, v14, v15
	global_store_dwordx4 v[12:13], v[8:11], off sc1
	v_mad_i64_i32 v[2:3], s[58:59], v7, s35, v[2:3]
	s_nop 0
	v_pk_mul_f32 v[8:9], v[46:47], s[38:39] op_sel_hi:[1,0]
	v_pk_mul_f32 v[10:11], v[48:49], s[38:39] op_sel_hi:[1,0]
	v_cvt_pk_bf16_f32 v8, v8, v9
	v_pk_mul_f32 v[14:15], v[44:45], s[38:39] op_sel_hi:[1,0]
	v_cvt_pk_bf16_f32 v9, v10, v11
	v_pk_mul_f32 v[16:17], v[42:43], s[38:39] op_sel_hi:[1,0]
	s_nop 0
	v_cvt_pk_bf16_f32 v10, v16, v17
	v_cvt_pk_bf16_f32 v11, v14, v15
	global_store_dwordx4 v[12:13], v[8:11], off offset:256 sc1
	v_pk_mul_f32 v[12:13], v[50:51], s[38:39] op_sel_hi:[1,0]
	s_nop 0
	v_lshl_add_u64 v[8:9], v[2:3], 0, v[4:5]
	v_pk_mul_f32 v[4:5], v[56:57], s[38:39] op_sel_hi:[1,0]
	v_pk_mul_f32 v[2:3], v[54:55], s[38:39] op_sel_hi:[1,0]
	v_pk_mul_f32 v[10:11], v[52:53], s[38:39] op_sel_hi:[1,0]
	v_cvt_pk_bf16_f32 v2, v2, v3
	v_cvt_pk_bf16_f32 v3, v4, v5
	v_cvt_pk_bf16_f32 v4, v12, v13
	v_pk_mul_f32 v[12:13], v[34:35], s[38:39] op_sel_hi:[1,0]
	v_cvt_pk_bf16_f32 v5, v10, v11
	global_store_dwordx4 v[8:9], v[2:5], off sc1
	v_pk_mul_f32 v[10:11], v[36:37], s[38:39] op_sel_hi:[1,0]
	s_nop 0
	v_pk_mul_f32 v[4:5], v[40:41], s[38:39] op_sel_hi:[1,0]
	v_pk_mul_f32 v[2:3], v[38:39], s[38:39] op_sel_hi:[1,0]
	s_nop 0
	v_cvt_pk_bf16_f32 v2, v2, v3
	v_cvt_pk_bf16_f32 v3, v4, v5
	v_cvt_pk_bf16_f32 v4, v12, v13
	v_cvt_pk_bf16_f32 v5, v10, v11
	global_store_dwordx4 v[8:9], v[2:5], off offset:256 sc1
	s_cbranch_execnz .LBB0_290
.LBB0_294:
	s_nop 0
	v_pk_mul_f32 v[4:5], v[158:159], s[40:41] op_sel_hi:[1,0]
	v_or_b32_e32 v2, v6, v199
	v_med3_f32 v6, v4, s30, v205
	v_med3_f32 v5, v5, s30, v205
	v_mov_b32_e32 v4, 0
	v_cvt_pk_fp8_f32 v4, v6, v5
	v_pk_mul_f32 v[6:7], v[160:161], s[40:41] op_sel_hi:[1,0]
	s_and_b64 s[58:59], s[56:57], exec
	v_med3_f32 v5, v6, s30, v205
	v_med3_f32 v6, v7, s30, v205
	v_cvt_pk_fp8_f32 v4, v5, v6 op_sel:[0,0,1]
	v_pk_mul_f32 v[6:7], v[154:155], s[40:41] op_sel_hi:[1,0]
	v_mov_b32_e32 v5, 0
	v_med3_f32 v6, v6, s30, v205
	v_med3_f32 v7, v7, s30, v205
	v_cvt_pk_fp8_f32 v5, v6, v7
	v_pk_mul_f32 v[6:7], v[156:157], s[40:41] op_sel_hi:[1,0]
	s_mov_b32 s18, 0xbe000000
	v_med3_f32 v6, v6, s30, v205
	v_med3_f32 v7, v7, s30, v205
	v_cvt_pk_fp8_f32 v5, v6, v7 op_sel:[0,0,1]
	v_pk_mul_f32 v[6:7], v[150:151], s[40:41] op_sel_hi:[1,0]
	s_cselect_b32 s18, s18, 0xc0400000
	v_med3_f32 v8, v6, s30, v205
	v_med3_f32 v7, v7, s30, v205
	v_mov_b32_e32 v6, 0
	v_cvt_pk_fp8_f32 v6, v8, v7
	v_pk_mul_f32 v[8:9], v[152:153], s[40:41] op_sel_hi:[1,0]
	s_add_u32 s58, s26, s18
	v_med3_f32 v7, v8, s30, v205
	v_med3_f32 v8, v9, s30, v205
	v_cvt_pk_fp8_f32 v6, v7, v8 op_sel:[0,0,1]
	v_pk_mul_f32 v[8:9], v[146:147], s[40:41] op_sel_hi:[1,0]
	v_mov_b32_e32 v7, 0
	v_med3_f32 v8, v8, s30, v205
	v_med3_f32 v9, v9, s30, v205
	s_addc_u32 s59, s27, 0
	v_cvt_pk_fp8_f32 v7, v8, v9
	s_and_b64 s[56:57], s[56:57], exec
	s_cselect_b32 s18, 0xffffffe0, -16
	v_pk_mul_f32 v[8:9], v[148:149], s[40:41] op_sel_hi:[1,0]
	v_ashrrev_i32_e32 v3, 31, v2
	s_cselect_b32 s43, 12, 11
	s_add_i32 s18, s18, s54
	v_med3_f32 v8, v8, s30, v205
	v_med3_f32 v9, v9, s30, v205
	v_lshlrev_b64 v[2:3], s43, v[2:3]
	s_lshl_b32 s56, s18, 8
	v_cvt_pk_fp8_f32 v7, v8, v9 op_sel:[0,0,1]
	v_lshl_add_u64 v[2:3], s[58:59], 0, v[2:3]
	s_ashr_i32 s57, s56, 31
	v_lshl_add_u64 v[2:3], v[2:3], 0, s[56:57]
	v_lshl_add_u64 v[2:3], v[2:3], 0, s[10:11]
	v_lshl_add_u64 v[2:3], v[2:3], 0, v[170:171]
	v_permlane16_swap_b32_e32 v4, v6
	v_permlane16_swap_b32_e32 v5, v7
	global_store_dwordx4 v[2:3], v[4:7], off sc1
	s_lshl_b64 s[56:57], 32, s43
	s_nop 0
	v_pk_mul_f32 v[4:5], v[142:143], s[40:41] op_sel_hi:[1,0]
	s_nop 0
	v_med3_f32 v6, v4, s30, v205
	v_med3_f32 v5, v5, s30, v205
	v_mov_b32_e32 v4, 0
	v_cvt_pk_fp8_f32 v4, v6, v5
	v_pk_mul_f32 v[6:7], v[144:145], s[40:41] op_sel_hi:[1,0]
	s_nop 0
	v_med3_f32 v5, v6, s30, v205
	v_med3_f32 v6, v7, s30, v205
	v_cvt_pk_fp8_f32 v4, v5, v6 op_sel:[0,0,1]
	v_pk_mul_f32 v[6:7], v[138:139], s[40:41] op_sel_hi:[1,0]
	v_mov_b32_e32 v5, 0
	v_med3_f32 v6, v6, s30, v205
	v_med3_f32 v7, v7, s30, v205
	v_cvt_pk_fp8_f32 v5, v6, v7
	v_pk_mul_f32 v[6:7], v[140:141], s[40:41] op_sel_hi:[1,0]
	s_nop 0
	v_med3_f32 v6, v6, s30, v205
	v_med3_f32 v7, v7, s30, v205
	v_cvt_pk_fp8_f32 v5, v6, v7 op_sel:[0,0,1]
	v_pk_mul_f32 v[6:7], v[134:135], s[40:41] op_sel_hi:[1,0]
	s_nop 0
	v_med3_f32 v8, v6, s30, v205
	v_med3_f32 v7, v7, s30, v205
	v_mov_b32_e32 v6, 0
	v_cvt_pk_fp8_f32 v6, v8, v7
	v_pk_mul_f32 v[8:9], v[136:137], s[40:41] op_sel_hi:[1,0]
	s_nop 0
	v_med3_f32 v7, v8, s30, v205
	v_med3_f32 v8, v9, s30, v205
	v_cvt_pk_fp8_f32 v6, v7, v8 op_sel:[0,0,1]
	v_pk_mul_f32 v[8:9], v[126:127], s[40:41] op_sel_hi:[1,0]
	v_mov_b32_e32 v7, 0
	v_med3_f32 v8, v8, s30, v205
	v_med3_f32 v9, v9, s30, v205
	v_cvt_pk_fp8_f32 v7, v8, v9
	v_pk_mul_f32 v[8:9], v[128:129], s[40:41] op_sel_hi:[1,0]
	v_permlane16_swap_b32_e32 v4, v6
	v_med3_f32 v8, v8, s30, v205
	v_med3_f32 v9, v9, s30, v205
	v_cvt_pk_fp8_f32 v7, v8, v9 op_sel:[0,0,1]
	v_lshl_add_u64 v[8:9], v[2:3], 0, s[56:57]
	s_lshl_b64 s[56:57], 0x80, s43
	v_permlane16_swap_b32_e32 v5, v7
	global_store_dwordx4 v[2:3], v[4:7], off offset:128 sc1
	s_nop 1
	v_pk_mul_f32 v[4:5], v[130:131], s[40:41] op_sel_hi:[1,0]
	s_nop 0
	v_med3_f32 v6, v4, s30, v205
	v_med3_f32 v5, v5, s30, v205
	v_mov_b32_e32 v4, 0
	v_cvt_pk_fp8_f32 v4, v6, v5
	v_pk_mul_f32 v[6:7], v[132:133], s[40:41] op_sel_hi:[1,0]
	s_nop 0
	v_med3_f32 v5, v6, s30, v205
	v_med3_f32 v6, v7, s30, v205
	v_cvt_pk_fp8_f32 v4, v5, v6 op_sel:[0,0,1]
	v_pk_mul_f32 v[6:7], v[122:123], s[40:41] op_sel_hi:[1,0]
	v_mov_b32_e32 v5, 0
	v_med3_f32 v6, v6, s30, v205
	v_med3_f32 v7, v7, s30, v205
	v_cvt_pk_fp8_f32 v5, v6, v7
	v_pk_mul_f32 v[6:7], v[124:125], s[40:41] op_sel_hi:[1,0]
	s_nop 0
	v_med3_f32 v6, v6, s30, v205
	v_med3_f32 v7, v7, s30, v205
	v_cvt_pk_fp8_f32 v5, v6, v7 op_sel:[0,0,1]
	v_pk_mul_f32 v[6:7], v[118:119], s[40:41] op_sel_hi:[1,0]
	s_nop 0
	v_med3_f32 v10, v6, s30, v205
	v_med3_f32 v7, v7, s30, v205
	v_mov_b32_e32 v6, 0
	v_cvt_pk_fp8_f32 v6, v10, v7
	v_pk_mul_f32 v[10:11], v[120:121], s[40:41] op_sel_hi:[1,0]
	s_nop 0
	v_med3_f32 v7, v10, s30, v205
	v_med3_f32 v10, v11, s30, v205
	v_cvt_pk_fp8_f32 v6, v7, v10 op_sel:[0,0,1]
	v_pk_mul_f32 v[10:11], v[114:115], s[40:41] op_sel_hi:[1,0]
	v_mov_b32_e32 v7, 0
	v_med3_f32 v10, v10, s30, v205
	v_med3_f32 v11, v11, s30, v205
	v_cvt_pk_fp8_f32 v7, v10, v11
	v_pk_mul_f32 v[10:11], v[116:117], s[40:41] op_sel_hi:[1,0]
	v_permlane16_swap_b32_e32 v4, v6
	v_med3_f32 v10, v10, s30, v205
	v_med3_f32 v11, v11, s30, v205
	v_cvt_pk_fp8_f32 v7, v10, v11 op_sel:[0,0,1]
	s_nop 1
	v_permlane16_swap_b32_e32 v5, v7
	global_store_dwordx4 v[8:9], v[4:7], off sc1
	s_nop 1
	v_pk_mul_f32 v[4:5], v[110:111], s[40:41] op_sel_hi:[1,0]
	s_nop 0
	v_med3_f32 v6, v4, s30, v205
	v_med3_f32 v5, v5, s30, v205
	v_mov_b32_e32 v4, 0
	v_cvt_pk_fp8_f32 v4, v6, v5
	v_pk_mul_f32 v[6:7], v[112:113], s[40:41] op_sel_hi:[1,0]
	s_nop 0
	v_med3_f32 v5, v6, s30, v205
	v_med3_f32 v6, v7, s30, v205
	v_cvt_pk_fp8_f32 v4, v5, v6 op_sel:[0,0,1]
	v_pk_mul_f32 v[6:7], v[106:107], s[40:41] op_sel_hi:[1,0]
	v_mov_b32_e32 v5, 0
	v_med3_f32 v6, v6, s30, v205
	v_med3_f32 v7, v7, s30, v205
	v_cvt_pk_fp8_f32 v5, v6, v7
	v_pk_mul_f32 v[6:7], v[108:109], s[40:41] op_sel_hi:[1,0]
	s_nop 0
	v_med3_f32 v6, v6, s30, v205
	v_med3_f32 v7, v7, s30, v205
	v_cvt_pk_fp8_f32 v5, v6, v7 op_sel:[0,0,1]
	v_pk_mul_f32 v[6:7], v[102:103], s[40:41] op_sel_hi:[1,0]
	s_nop 0
	v_med3_f32 v10, v6, s30, v205
	v_med3_f32 v7, v7, s30, v205
	v_mov_b32_e32 v6, 0
	v_cvt_pk_fp8_f32 v6, v10, v7
	v_pk_mul_f32 v[10:11], v[104:105], s[40:41] op_sel_hi:[1,0]
	s_nop 0
	v_med3_f32 v7, v10, s30, v205
	v_med3_f32 v10, v11, s30, v205
	v_cvt_pk_fp8_f32 v6, v7, v10 op_sel:[0,0,1]
	v_pk_mul_f32 v[10:11], v[98:99], s[40:41] op_sel_hi:[1,0]
	v_mov_b32_e32 v7, 0
	v_med3_f32 v10, v10, s30, v205
	v_med3_f32 v11, v11, s30, v205
	v_cvt_pk_fp8_f32 v7, v10, v11
	v_pk_mul_f32 v[10:11], v[100:101], s[40:41] op_sel_hi:[1,0]
	v_permlane16_swap_b32_e32 v4, v6
	v_med3_f32 v10, v10, s30, v205
	v_med3_f32 v11, v11, s30, v205
	v_cvt_pk_fp8_f32 v7, v10, v11 op_sel:[0,0,1]
	s_nop 1
	v_permlane16_swap_b32_e32 v5, v7
	global_store_dwordx4 v[8:9], v[4:7], off offset:128 sc1
	v_lshl_add_u64 v[8:9], v[2:3], 0, s[56:57]
	s_lshl_b64 s[56:57], 0xa0, s43
	v_pk_mul_f32 v[4:5], v[94:95], s[40:41] op_sel_hi:[1,0]
	s_nop 0
	v_med3_f32 v6, v4, s30, v205
	v_med3_f32 v5, v5, s30, v205
	v_mov_b32_e32 v4, 0
	v_cvt_pk_fp8_f32 v4, v6, v5
	v_pk_mul_f32 v[6:7], v[96:97], s[40:41] op_sel_hi:[1,0]
	s_nop 0
	v_med3_f32 v5, v6, s30, v205
	v_med3_f32 v6, v7, s30, v205
	v_cvt_pk_fp8_f32 v4, v5, v6 op_sel:[0,0,1]
	v_pk_mul_f32 v[6:7], v[90:91], s[40:41] op_sel_hi:[1,0]
	v_mov_b32_e32 v5, 0
	v_med3_f32 v6, v6, s30, v205
	v_med3_f32 v7, v7, s30, v205
	v_cvt_pk_fp8_f32 v5, v6, v7
	v_pk_mul_f32 v[6:7], v[92:93], s[40:41] op_sel_hi:[1,0]
	s_nop 0
	v_med3_f32 v6, v6, s30, v205
	v_med3_f32 v7, v7, s30, v205
	v_cvt_pk_fp8_f32 v5, v6, v7 op_sel:[0,0,1]
	v_pk_mul_f32 v[6:7], v[86:87], s[40:41] op_sel_hi:[1,0]
	s_nop 0
	v_med3_f32 v10, v6, s30, v205
	v_med3_f32 v7, v7, s30, v205
	v_mov_b32_e32 v6, 0
	v_cvt_pk_fp8_f32 v6, v10, v7
	v_pk_mul_f32 v[10:11], v[88:89], s[40:41] op_sel_hi:[1,0]
	s_nop 0
	v_med3_f32 v7, v10, s30, v205
	v_med3_f32 v10, v11, s30, v205
	v_cvt_pk_fp8_f32 v6, v7, v10 op_sel:[0,0,1]
	v_pk_mul_f32 v[10:11], v[82:83], s[40:41] op_sel_hi:[1,0]
	v_mov_b32_e32 v7, 0
	v_med3_f32 v10, v10, s30, v205
	v_med3_f32 v11, v11, s30, v205
	v_cvt_pk_fp8_f32 v7, v10, v11
	v_pk_mul_f32 v[10:11], v[84:85], s[40:41] op_sel_hi:[1,0]
	v_permlane16_swap_b32_e32 v4, v6
	v_med3_f32 v10, v10, s30, v205
	v_med3_f32 v11, v11, s30, v205
	v_cvt_pk_fp8_f32 v7, v10, v11 op_sel:[0,0,1]
	s_nop 1
	v_permlane16_swap_b32_e32 v5, v7
	global_store_dwordx4 v[8:9], v[4:7], off sc1
	s_nop 1
	v_pk_mul_f32 v[4:5], v[78:79], s[40:41] op_sel_hi:[1,0]
	s_nop 0
	v_med3_f32 v6, v4, s30, v205
	v_med3_f32 v5, v5, s30, v205
	v_mov_b32_e32 v4, 0
	v_cvt_pk_fp8_f32 v4, v6, v5
	v_pk_mul_f32 v[6:7], v[80:81], s[40:41] op_sel_hi:[1,0]
	s_nop 0
	v_med3_f32 v5, v6, s30, v205
	v_med3_f32 v6, v7, s30, v205
	v_cvt_pk_fp8_f32 v4, v5, v6 op_sel:[0,0,1]
	v_pk_mul_f32 v[6:7], v[74:75], s[40:41] op_sel_hi:[1,0]
	v_mov_b32_e32 v5, 0
	v_med3_f32 v6, v6, s30, v205
	v_med3_f32 v7, v7, s30, v205
	v_cvt_pk_fp8_f32 v5, v6, v7
	v_pk_mul_f32 v[6:7], v[76:77], s[40:41] op_sel_hi:[1,0]
	s_nop 0
	v_med3_f32 v6, v6, s30, v205
	v_med3_f32 v7, v7, s30, v205
	v_cvt_pk_fp8_f32 v5, v6, v7 op_sel:[0,0,1]
	v_pk_mul_f32 v[6:7], v[70:71], s[40:41] op_sel_hi:[1,0]
	s_nop 0
	v_med3_f32 v10, v6, s30, v205
	v_med3_f32 v7, v7, s30, v205
	v_mov_b32_e32 v6, 0
	v_cvt_pk_fp8_f32 v6, v10, v7
	v_pk_mul_f32 v[10:11], v[72:73], s[40:41] op_sel_hi:[1,0]
	s_nop 0
	v_med3_f32 v7, v10, s30, v205
	v_med3_f32 v10, v11, s30, v205
	v_cvt_pk_fp8_f32 v6, v7, v10 op_sel:[0,0,1]
	v_pk_mul_f32 v[10:11], v[62:63], s[40:41] op_sel_hi:[1,0]
	v_mov_b32_e32 v7, 0
	v_med3_f32 v10, v10, s30, v205
	v_med3_f32 v11, v11, s30, v205
	v_cvt_pk_fp8_f32 v7, v10, v11
	v_pk_mul_f32 v[10:11], v[64:65], s[40:41] op_sel_hi:[1,0]
	v_permlane16_swap_b32_e32 v4, v6
	v_med3_f32 v10, v10, s30, v205
	v_med3_f32 v11, v11, s30, v205
	v_cvt_pk_fp8_f32 v7, v10, v11 op_sel:[0,0,1]
	s_nop 1
	v_permlane16_swap_b32_e32 v5, v7
	global_store_dwordx4 v[8:9], v[4:7], off offset:128 sc1
	s_nop 1
	v_lshl_add_u64 v[6:7], v[2:3], 0, s[56:57]
	v_pk_mul_f32 v[2:3], v[66:67], s[40:41] op_sel_hi:[1,0]
	s_nop 0
	v_med3_f32 v4, v2, s30, v205
	v_med3_f32 v3, v3, s30, v205
	v_mov_b32_e32 v2, 0
	v_cvt_pk_fp8_f32 v2, v4, v3
	v_pk_mul_f32 v[4:5], v[68:69], s[40:41] op_sel_hi:[1,0]
	s_nop 0
	v_med3_f32 v3, v4, s30, v205
	v_med3_f32 v4, v5, s30, v205
	v_cvt_pk_fp8_f32 v2, v3, v4 op_sel:[0,0,1]
	v_pk_mul_f32 v[4:5], v[58:59], s[40:41] op_sel_hi:[1,0]
	v_mov_b32_e32 v3, 0
	v_med3_f32 v4, v4, s30, v205
	v_med3_f32 v5, v5, s30, v205
	v_cvt_pk_fp8_f32 v3, v4, v5
	v_pk_mul_f32 v[4:5], v[60:61], s[40:41] op_sel_hi:[1,0]
	s_nop 0
	v_med3_f32 v4, v4, s30, v205
	v_med3_f32 v5, v5, s30, v205
	v_cvt_pk_fp8_f32 v3, v4, v5 op_sel:[0,0,1]
	v_pk_mul_f32 v[4:5], v[54:55], s[40:41] op_sel_hi:[1,0]
	s_nop 0
	v_med3_f32 v8, v4, s30, v205
	v_med3_f32 v5, v5, s30, v205
	v_mov_b32_e32 v4, 0
	v_cvt_pk_fp8_f32 v4, v8, v5
	v_pk_mul_f32 v[8:9], v[56:57], s[40:41] op_sel_hi:[1,0]
	s_nop 0
	v_med3_f32 v5, v8, s30, v205
	v_med3_f32 v8, v9, s30, v205
	v_cvt_pk_fp8_f32 v4, v5, v8 op_sel:[0,0,1]
	v_pk_mul_f32 v[8:9], v[50:51], s[40:41] op_sel_hi:[1,0]
	v_mov_b32_e32 v5, 0
	v_med3_f32 v8, v8, s30, v205
	v_med3_f32 v9, v9, s30, v205
	v_cvt_pk_fp8_f32 v5, v8, v9
	v_pk_mul_f32 v[8:9], v[52:53], s[40:41] op_sel_hi:[1,0]
	v_permlane16_swap_b32_e32 v2, v4
	v_med3_f32 v8, v8, s30, v205
	v_med3_f32 v9, v9, s30, v205
	v_cvt_pk_fp8_f32 v5, v8, v9 op_sel:[0,0,1]
	s_nop 1
	v_permlane16_swap_b32_e32 v3, v5
	global_store_dwordx4 v[6:7], v[2:5], off sc1
	s_nop 1
	v_pk_mul_f32 v[2:3], v[46:47], s[40:41] op_sel_hi:[1,0]
	s_nop 0
	v_med3_f32 v4, v2, s30, v205
	v_med3_f32 v3, v3, s30, v205
	v_mov_b32_e32 v2, 0
	v_cvt_pk_fp8_f32 v2, v4, v3
	v_pk_mul_f32 v[4:5], v[48:49], s[40:41] op_sel_hi:[1,0]
	s_nop 0
	v_med3_f32 v3, v4, s30, v205
	v_med3_f32 v4, v5, s30, v205
	v_cvt_pk_fp8_f32 v2, v3, v4 op_sel:[0,0,1]
	v_pk_mul_f32 v[4:5], v[42:43], s[40:41] op_sel_hi:[1,0]
	v_mov_b32_e32 v3, 0
	v_med3_f32 v4, v4, s30, v205
	v_med3_f32 v5, v5, s30, v205
	v_cvt_pk_fp8_f32 v3, v4, v5
	v_pk_mul_f32 v[4:5], v[44:45], s[40:41] op_sel_hi:[1,0]
	s_nop 0
	v_med3_f32 v4, v4, s30, v205
	v_med3_f32 v5, v5, s30, v205
	v_cvt_pk_fp8_f32 v3, v4, v5 op_sel:[0,0,1]
	v_pk_mul_f32 v[4:5], v[38:39], s[40:41] op_sel_hi:[1,0]
	s_nop 0
	v_med3_f32 v8, v4, s30, v205
	v_med3_f32 v5, v5, s30, v205
	v_mov_b32_e32 v4, 0
	v_cvt_pk_fp8_f32 v4, v8, v5
	v_pk_mul_f32 v[8:9], v[40:41], s[40:41] op_sel_hi:[1,0]
	s_nop 0
	v_med3_f32 v5, v8, s30, v205
	v_med3_f32 v8, v9, s30, v205
	v_cvt_pk_fp8_f32 v4, v5, v8 op_sel:[0,0,1]
	v_pk_mul_f32 v[8:9], v[34:35], s[40:41] op_sel_hi:[1,0]
	v_mov_b32_e32 v5, 0
	v_med3_f32 v8, v8, s30, v205
	v_med3_f32 v9, v9, s30, v205
	v_cvt_pk_fp8_f32 v5, v8, v9
	v_pk_mul_f32 v[8:9], v[36:37], s[40:41] op_sel_hi:[1,0]
	v_permlane16_swap_b32_e32 v2, v4
	v_med3_f32 v8, v8, s30, v205
	v_med3_f32 v9, v9, s30, v205
	v_cvt_pk_fp8_f32 v5, v8, v9 op_sel:[0,0,1]
	s_nop 1
	v_permlane16_swap_b32_e32 v3, v5
	global_store_dwordx4 v[6:7], v[2:5], off offset:128 sc1
	s_andn2_b64 vcc, exec, s[46:47]
	s_cbranch_vccz .LBB0_291

.LBB0_339:
	s_mul_hi_i32 s17, s86, 0x92492493
	s_add_i32 s17, s17, s86
	s_lshr_b32 s18, s17, 31
	s_lshr_b32 s17, s17, 5
	s_add_i32 s17, s17, s18
	s_mul_i32 s17, s17, 56
	s_sub_i32 s17, s86, s17
	v_lshl_or_b32 v144, s17, 8, v148
	v_lshl_add_u32 v151, s46, 8, v146
	v_ashrrev_i32_e32 v145, 31, v144
	v_mov_b64_e32 v[142:143], s[0:1]
	v_mad_i64_i32 v[152:153], s[48:49], v151, s85, v[142:143]
	v_lshlrev_b64 v[144:145], 1, v[144:145]
	v_lshl_add_u64 v[152:153], v[152:153], 0, v[144:145]
	v_pk_add_f32 v[128:129], v[128:129], 0 op_sel_hi:[1,0]
	v_pk_add_f32 v[126:127], v[126:127], 0 op_sel_hi:[1,0]
	v_pk_add_f32 v[154:155], v[124:125], 0 op_sel_hi:[1,0]
	v_pk_add_f32 v[124:125], v[122:123], 0 op_sel_hi:[1,0]
	v_cvt_pk_bf16_f32 v122, v126, v127
	v_cvt_pk_bf16_f32 v123, v128, v129
	v_pk_add_f32 v[118:119], v[118:119], 0 op_sel_hi:[1,0]
	v_cvt_pk_bf16_f32 v124, v124, v125
	v_cvt_pk_bf16_f32 v125, v154, v155
	global_store_dwordx4 v[152:153], v[122:125], off sc1
	v_pk_add_f32 v[120:121], v[120:121], 0 op_sel_hi:[1,0]
	v_pk_add_f32 v[114:115], v[114:115], 0 op_sel_hi:[1,0]
	v_pk_add_f32 v[122:123], v[112:113], 0 op_sel_hi:[1,0]
	v_pk_add_f32 v[112:113], v[110:111], 0 op_sel_hi:[1,0]
	v_cvt_pk_bf16_f32 v110, v118, v119
	v_cvt_pk_bf16_f32 v111, v120, v121
	v_pk_add_f32 v[102:103], v[102:103], 0 op_sel_hi:[1,0]
	v_cvt_pk_bf16_f32 v112, v112, v113
	v_cvt_pk_bf16_f32 v113, v122, v123
	global_store_dwordx4 v[152:153], v[110:113], off offset:256 sc1
	v_pk_add_f32 v[104:105], v[104:105], 0 op_sel_hi:[1,0]
	v_pk_add_f32 v[98:99], v[98:99], 0 op_sel_hi:[1,0]
	v_or_b32_e32 v110, 16, v151
	v_mad_i64_i32 v[110:111], s[48:49], v110, s85, v[142:143]
	v_lshl_add_u64 v[110:111], v[110:111], 0, v[144:145]
	v_pk_add_f32 v[112:113], v[116:117], 0 op_sel_hi:[1,0]
	v_pk_add_f32 v[116:117], v[108:109], 0 op_sel_hi:[1,0]
	v_pk_add_f32 v[108:109], v[106:107], 0 op_sel_hi:[1,0]
	v_cvt_pk_bf16_f32 v106, v114, v115
	v_cvt_pk_bf16_f32 v107, v112, v113
	v_pk_add_f32 v[86:87], v[86:87], 0 op_sel_hi:[1,0]
	v_cvt_pk_bf16_f32 v108, v108, v109
	v_cvt_pk_bf16_f32 v109, v116, v117
	global_store_dwordx4 v[110:111], v[106:109], off sc1
	v_pk_add_f32 v[88:89], v[88:89], 0 op_sel_hi:[1,0]
	v_pk_add_f32 v[82:83], v[82:83], 0 op_sel_hi:[1,0]
	v_pk_add_f32 v[106:107], v[96:97], 0 op_sel_hi:[1,0]
	v_pk_add_f32 v[96:97], v[94:95], 0 op_sel_hi:[1,0]
	v_cvt_pk_bf16_f32 v94, v102, v103
	v_cvt_pk_bf16_f32 v95, v104, v105
	v_pk_add_f32 v[70:71], v[70:71], 0 op_sel_hi:[1,0]
	v_cvt_pk_bf16_f32 v96, v96, v97
	v_cvt_pk_bf16_f32 v97, v106, v107
	global_store_dwordx4 v[110:111], v[94:97], off offset:256 sc1
	v_pk_add_f32 v[72:73], v[72:73], 0 op_sel_hi:[1,0]
	v_pk_add_f32 v[64:65], v[64:65], 0 op_sel_hi:[1,0]
	v_or_b32_e32 v94, 32, v151
	v_mad_i64_i32 v[94:95], s[48:49], v94, s85, v[142:143]
	v_lshl_add_u64 v[94:95], v[94:95], 0, v[144:145]
	v_pk_add_f32 v[96:97], v[100:101], 0 op_sel_hi:[1,0]
	v_pk_add_f32 v[100:101], v[92:93], 0 op_sel_hi:[1,0]
	v_pk_add_f32 v[92:93], v[90:91], 0 op_sel_hi:[1,0]
	v_cvt_pk_bf16_f32 v90, v98, v99
	v_cvt_pk_bf16_f32 v91, v96, v97
	v_pk_add_f32 v[62:63], v[62:63], 0 op_sel_hi:[1,0]
	v_cvt_pk_bf16_f32 v92, v92, v93
	v_cvt_pk_bf16_f32 v93, v100, v101
	global_store_dwordx4 v[94:95], v[90:93], off sc1
	v_pk_add_f32 v[54:55], v[54:55], 0 op_sel_hi:[1,0]
	v_pk_add_f32 v[56:57], v[56:57], 0 op_sel_hi:[1,0]
	v_pk_add_f32 v[90:91], v[80:81], 0 op_sel_hi:[1,0]
	v_pk_add_f32 v[80:81], v[78:79], 0 op_sel_hi:[1,0]
	v_cvt_pk_bf16_f32 v78, v86, v87
	v_cvt_pk_bf16_f32 v79, v88, v89
	v_pk_add_f32 v[50:51], v[50:51], 0 op_sel_hi:[1,0]
	v_cvt_pk_bf16_f32 v80, v80, v81
	v_cvt_pk_bf16_f32 v81, v90, v91
	global_store_dwordx4 v[94:95], v[78:81], off offset:256 sc1
	v_pk_add_f32 v[38:39], v[38:39], 0 op_sel_hi:[1,0]
	v_pk_add_f32 v[40:41], v[40:41], 0 op_sel_hi:[1,0]
	v_or_b32_e32 v78, 48, v151
	v_mad_i64_i32 v[78:79], s[48:49], v78, s85, v[142:143]
	v_lshl_add_u64 v[78:79], v[78:79], 0, v[144:145]
	v_pk_add_f32 v[80:81], v[84:85], 0 op_sel_hi:[1,0]
	v_pk_add_f32 v[84:85], v[76:77], 0 op_sel_hi:[1,0]
	v_pk_add_f32 v[76:77], v[74:75], 0 op_sel_hi:[1,0]
	v_cvt_pk_bf16_f32 v74, v82, v83
	v_cvt_pk_bf16_f32 v75, v80, v81
	v_pk_add_f32 v[34:35], v[34:35], 0 op_sel_hi:[1,0]
	v_cvt_pk_bf16_f32 v76, v76, v77
	v_cvt_pk_bf16_f32 v77, v84, v85
	global_store_dwordx4 v[78:79], v[74:77], off sc1
	v_pk_add_f32 v[22:23], v[22:23], 0 op_sel_hi:[1,0]
	v_pk_add_f32 v[24:25], v[24:25], 0 op_sel_hi:[1,0]
	v_pk_add_f32 v[74:75], v[68:69], 0 op_sel_hi:[1,0]
	v_pk_add_f32 v[68:69], v[66:67], 0 op_sel_hi:[1,0]
	v_cvt_pk_bf16_f32 v66, v70, v71
	v_cvt_pk_bf16_f32 v67, v72, v73
	v_pk_add_f32 v[18:19], v[18:19], 0 op_sel_hi:[1,0]
	v_cvt_pk_bf16_f32 v68, v68, v69
	v_cvt_pk_bf16_f32 v69, v74, v75
	global_store_dwordx4 v[78:79], v[66:69], off offset:256 sc1
	s_andn2_b64 vcc, exec, s[42:43]
	v_pk_add_f32 v[8:9], v[8:9], 0 op_sel_hi:[1,0]
	v_add_u32_e32 v66, 0x80, v151
	v_mad_i64_i32 v[66:67], s[48:49], v66, s85, v[142:143]
	v_lshl_add_u64 v[66:67], v[66:67], 0, v[144:145]
	v_pk_add_f32 v[68:69], v[60:61], 0 op_sel_hi:[1,0]
	v_pk_add_f32 v[60:61], v[58:59], 0 op_sel_hi:[1,0]
	v_cvt_pk_bf16_f32 v58, v62, v63
	v_cvt_pk_bf16_f32 v59, v64, v65
	v_pk_add_f32 v[6:7], v[6:7], 0 op_sel_hi:[1,0]
	v_cvt_pk_bf16_f32 v60, v60, v61
	v_cvt_pk_bf16_f32 v61, v68, v69
	global_store_dwordx4 v[66:67], v[58:61], off sc1
	s_nop 1
	v_pk_add_f32 v[58:59], v[48:49], 0 op_sel_hi:[1,0]
	v_pk_add_f32 v[48:49], v[46:47], 0 op_sel_hi:[1,0]
	v_cvt_pk_bf16_f32 v46, v54, v55
	v_cvt_pk_bf16_f32 v47, v56, v57
	s_nop 0
	v_cvt_pk_bf16_f32 v48, v48, v49
	v_cvt_pk_bf16_f32 v49, v58, v59
	global_store_dwordx4 v[66:67], v[46:49], off offset:256 sc1
	s_nop 1
	v_add_u32_e32 v46, 0x90, v151
	v_mad_i64_i32 v[46:47], s[48:49], v46, s85, v[142:143]
	v_lshl_add_u64 v[46:47], v[46:47], 0, v[144:145]
	v_pk_add_f32 v[48:49], v[52:53], 0 op_sel_hi:[1,0]
	v_pk_add_f32 v[52:53], v[44:45], 0 op_sel_hi:[1,0]
	v_pk_add_f32 v[44:45], v[42:43], 0 op_sel_hi:[1,0]
	v_cvt_pk_bf16_f32 v42, v50, v51
	v_cvt_pk_bf16_f32 v43, v48, v49
	s_nop 0
	v_cvt_pk_bf16_f32 v44, v44, v45
	v_cvt_pk_bf16_f32 v45, v52, v53
	global_store_dwordx4 v[46:47], v[42:45], off sc1
	s_nop 1
	v_pk_add_f32 v[42:43], v[32:33], 0 op_sel_hi:[1,0]
	v_pk_add_f32 v[32:33], v[30:31], 0 op_sel_hi:[1,0]
	v_cvt_pk_bf16_f32 v30, v38, v39
	v_cvt_pk_bf16_f32 v31, v40, v41
	s_nop 0
	v_cvt_pk_bf16_f32 v32, v32, v33
	v_cvt_pk_bf16_f32 v33, v42, v43
	global_store_dwordx4 v[46:47], v[30:33], off offset:256 sc1
	s_nop 1
	v_add_u32_e32 v30, 0xa0, v151
	v_mad_i64_i32 v[30:31], s[48:49], v30, s85, v[142:143]
	v_lshl_add_u64 v[30:31], v[30:31], 0, v[144:145]
	v_pk_add_f32 v[32:33], v[36:37], 0 op_sel_hi:[1,0]
	v_pk_add_f32 v[36:37], v[28:29], 0 op_sel_hi:[1,0]
	v_pk_add_f32 v[28:29], v[26:27], 0 op_sel_hi:[1,0]
	v_cvt_pk_bf16_f32 v26, v34, v35
	v_cvt_pk_bf16_f32 v27, v32, v33
	s_nop 0
	v_cvt_pk_bf16_f32 v28, v28, v29
	v_cvt_pk_bf16_f32 v29, v36, v37
	global_store_dwordx4 v[30:31], v[26:29], off sc1
	s_nop 1
	v_pk_add_f32 v[26:27], v[16:17], 0 op_sel_hi:[1,0]
	v_pk_add_f32 v[16:17], v[14:15], 0 op_sel_hi:[1,0]
	v_cvt_pk_bf16_f32 v14, v22, v23
	v_cvt_pk_bf16_f32 v15, v24, v25
	s_nop 0
	v_cvt_pk_bf16_f32 v16, v16, v17
	v_cvt_pk_bf16_f32 v17, v26, v27
	global_store_dwordx4 v[30:31], v[14:17], off offset:256 sc1
	s_nop 1
	v_add_u32_e32 v14, 0xb0, v151
	v_mad_i64_i32 v[14:15], s[48:49], v14, s85, v[142:143]
	v_lshl_add_u64 v[14:15], v[14:15], 0, v[144:145]
	v_pk_add_f32 v[16:17], v[20:21], 0 op_sel_hi:[1,0]
	v_pk_add_f32 v[20:21], v[12:13], 0 op_sel_hi:[1,0]
	v_pk_add_f32 v[12:13], v[10:11], 0 op_sel_hi:[1,0]
	v_cvt_pk_bf16_f32 v10, v18, v19
	v_cvt_pk_bf16_f32 v11, v16, v17
	s_nop 0
	v_cvt_pk_bf16_f32 v12, v12, v13
	v_cvt_pk_bf16_f32 v13, v20, v21
	global_store_dwordx4 v[14:15], v[10:13], off sc1
	s_nop 1
	v_pk_add_f32 v[10:11], v[4:5], 0 op_sel_hi:[1,0]
	v_pk_add_f32 v[4:5], v[2:3], 0 op_sel_hi:[1,0]
	v_cvt_pk_bf16_f32 v2, v6, v7
	v_cvt_pk_bf16_f32 v3, v8, v9
	s_nop 0
	v_cvt_pk_bf16_f32 v4, v4, v5
	v_cvt_pk_bf16_f32 v5, v10, v11
	global_store_dwordx4 v[14:15], v[2:5], off offset:256 sc1
	s_cbranch_vccnz .LBB0_342
	s_andn2_b64 vcc, exec, s[10:11]
	s_cbranch_vccnz .LBB0_315
	s_barrier
	s_branch .LBB0_315
